# P0 S5 unit: Bt_ssm output loop rewritten by hand as two wave-uniform passes (Toeplitz part: row per step, 64 lanes = 64 chunks; carry part: 4 rows per step) instead of 80 divergent iterations per thre
# baseline (speedup 1.0000x reference)
; DI unsigned pk2(float lo, float hi) { f32x2 v = {lo, hi}; bf16x2v r = __builtin_convertvector(v, bf16x2v); return __builtin_bit_cast(unsigned, r); }
; DI void p_ssm_unit(Frame& F, int unit) {
;     ...
;     bf16_t* bs = (bf16_t*)(F.ws + WS_BSSM) + (size_t)lg * 512 * UAK;
;     for (int o = F.tid; o < 512 * (UAK / 8); o += 512) { const int n = o / (UAK / 8), k8 = (o % (UAK / 8)) * 8; const int j = n >> 4, cc = n & 15; float v[8];
;         if (k8 < 512) { const int i = k8 >> 4, c0 = k8 & 15;
; #pragma unroll
;             for (int q = 0; q < 8; ++q) v[q] = (i <= j) ? Kt[((j - i) * 16 + cc) * 16 + c0 + q] : 0.f; }
;         else { const int p0 = (k8 - 512) >> 1;
; #pragma unroll
;             for (int q = 0; q < 4; ++q) { const int p = p0 + q; const float cr = Cc[(cc * 64 + p) * 2], ci = Cc[(cc * 64 + p) * 2 + 1]; const f32x2 lv = Lf[(j + 1) * 64 + p];
;                 v[2 * q] = cr * lv[0] - ci * lv[1]; v[2 * q + 1] = -(cr * lv[1] + ci * lv[0]); } }
;         u32x4 w; w.x = pk2(v[0], v[1]); w.y = pk2(v[2], v[3]); w.z = pk2(v[4], v[5]); w.w = pk2(v[6], v[7]);
;         *(u32x4*)(bs + (size_t)n * UAK + k8) = w; }
.LBB0_45:
	s_or_b64 exec, exec, s[4:5]
	v_lshlrev_b32_e32 v11, 6, v11
	v_lshlrev_b32_e32 v23, 2, v23
	v_add3_u32 v11, s34, v11, v23
	v_lshl_add_u32 v22, v22, 10, v11
	s_mov_b32 s4, 0xa000
	ds_write2st64_b32 v22, v2, v3 offset1:4
	ds_write2st64_b32 v22, v4, v5 offset0:8 offset1:12
	ds_write2st64_b32 v22, v6, v7 offset0:16 offset1:20
	ds_write2st64_b32 v22, v12, v13 offset0:24 offset1:28
	ds_write2st64_b32 v22, v14, v15 offset0:32 offset1:36
	ds_write2st64_b32 v22, v16, v17 offset0:40 offset1:44
	ds_write2st64_b32 v22, v18, v19 offset0:48 offset1:52
	ds_write_b32 v22, v0 offset:14336
	v_lshl_add_u32 v0, v8, 10, v11
	v_cmp_gt_i32_e32 vcc, s4, v10
	ds_write_b32 v0, v1
	s_waitcnt lgkmcnt(0)
	s_barrier
	s_and_saveexec_b64 s[4:5], vcc
	v_readlane_b32 s90, v253, 31
	v_readlane_b32 s91, v253, 32
	s_cbranch_execz .LBB0_68
	s_mul_i32 s6, s88, 0xa0000
	v_readlane_b32 s8, v253, 15
	s_mul_hi_i32 s7, s88, 0xa0000
	s_add_u32 s6, s8, s6
	v_readlane_b32 s8, v253, 17
	s_addc_u32 s7, s8, s7
	s_mul_i32 s8, s97, 0x14000
	s_add_u32 s6, s6, s8
	s_addc_u32 s7, s7, 0
	v_lshrrev_b32_e32 v22, 1, v20
	v_and_b32_e32 v23, 1, v20
	v_lshlrev_b32_e32 v24, 5, v23
	v_lshlrev_b32_e32 v25, 10, v22
	v_sub_u32_e32 v24, v24, v25
	v_lshlrev_b32_e32 v26, 4, v20
	s_lshl_b32 s9, s97, 2
	s_mov_b32 s8, 0
.Lp0_bssm_a:
	s_lshr_b32 s10, s8, 2
	s_add_i32 s10, s9, s10
	v_cmp_ge_i32_e32 vcc, s10, v22
	s_lshl_b32 s11, s10, 10
	s_and_b32 s10, s8, 3
	s_lshl_b32 s10, s10, 8
	s_add_i32 s11, s11, s10
	s_add_i32 s11, s11, 0x10400
	v_add_u32_e32 v27, s11, v24
	ds_read_b128 v[28:31], v27
	ds_read_b128 v[32:35], v27 offset:16
	ds_read_b128 v[36:39], v27 offset:64
	ds_read_b128 v[40:43], v27 offset:80
	ds_read_b128 v[44:47], v27 offset:128
	ds_read_b128 v[48:51], v27 offset:144
	ds_read_b128 v[52:55], v27 offset:192
	ds_read_b128 v[56:59], v27 offset:208
	s_waitcnt lgkmcnt(6)
	v_cvt_pk_bf16_f32 v28, v28, v29
	v_cvt_pk_bf16_f32 v29, v30, v31
	v_cvt_pk_bf16_f32 v30, v32, v33
	v_cvt_pk_bf16_f32 v31, v34, v35
	v_cndmask_b32_e32 v28, 0, v28, vcc
	v_cndmask_b32_e32 v29, 0, v29, vcc
	v_cndmask_b32_e32 v30, 0, v30, vcc
	v_cndmask_b32_e32 v31, 0, v31, vcc
	global_store_dwordx4 v26, v[28:31], s[6:7]
	s_waitcnt lgkmcnt(4)
	v_cvt_pk_bf16_f32 v36, v36, v37
	v_cvt_pk_bf16_f32 v37, v38, v39
	v_cvt_pk_bf16_f32 v38, v40, v41
	v_cvt_pk_bf16_f32 v39, v42, v43
	v_cndmask_b32_e32 v36, 0, v36, vcc
	v_cndmask_b32_e32 v37, 0, v37, vcc
	v_cndmask_b32_e32 v38, 0, v38, vcc
	v_cndmask_b32_e32 v39, 0, v39, vcc
	global_store_dwordx4 v26, v[36:39], s[6:7] offset:1280
	s_waitcnt lgkmcnt(2)
	v_cvt_pk_bf16_f32 v44, v44, v45
	v_cvt_pk_bf16_f32 v45, v46, v47
	v_cvt_pk_bf16_f32 v46, v48, v49
	v_cvt_pk_bf16_f32 v47, v50, v51
	v_cndmask_b32_e32 v44, 0, v44, vcc
	v_cndmask_b32_e32 v45, 0, v45, vcc
	v_cndmask_b32_e32 v46, 0, v46, vcc
	v_cndmask_b32_e32 v47, 0, v47, vcc
	global_store_dwordx4 v26, v[44:47], s[6:7] offset:2560
	s_waitcnt lgkmcnt(0)
	v_cvt_pk_bf16_f32 v52, v52, v53
	v_cvt_pk_bf16_f32 v53, v54, v55
	v_cvt_pk_bf16_f32 v54, v56, v57
	v_cvt_pk_bf16_f32 v55, v58, v59
	v_cndmask_b32_e32 v52, 0, v52, vcc
	v_cndmask_b32_e32 v53, 0, v53, vcc
	v_cndmask_b32_e32 v54, 0, v54, vcc
	v_cndmask_b32_e32 v55, 0, v55, vcc
	global_store_dwordx4 v26, v[52:55], s[6:7] offset:3840
	s_add_u32 s6, s6, 0x1400
	s_addc_u32 s7, s7, 0
	s_add_i32 s8, s8, 1
	s_cmp_lt_u32 s8, 16
	s_cbranch_scc1 .Lp0_bssm_a
	v_and_b32_e32 v60, 15, v20
	v_lshrrev_b32_e32 v61, 4, v20
	v_lshlrev_b32_e32 v62, 5, v60
	v_lshl_add_u32 v63, v61, 9, v62
	v_mul_u32_u24_e32 v64, 0x500, v61
	v_lshl_add_u32 v64, v60, 4, v64
	v_add_u32_e32 v64, 0x400, v64
	s_sub_u32 s6, s6, 0x14000
	s_subb_u32 s7, s7, 0
	s_mov_b32 s8, 0
.Lp0_bssm_b:
	s_lshr_b32 s10, s8, 2
	s_add_i32 s10, s9, s10
	s_lshl_b32 s10, s10, 9
	s_add_i32 s10, s10, 0x18600
	s_and_b32 s11, s8, 3
	s_lshl_b32 s11, s11, 11
	s_add_i32 s11, s11, 0xc400
	v_add_u32_e32 v65, s10, v62
	v_add_u32_e32 v66, s11, v63
	ds_read_b128 v[68:71], v66
	ds_read_b128 v[72:75], v65
	ds_read_b128 v[76:79], v66 offset:16
	ds_read_b128 v[80:83], v65 offset:16
	s_waitcnt lgkmcnt(2)
	v_mul_f32_e32 v84, v69, v73
	v_mul_f32_e32 v85, v69, v72
	v_fma_f32 v84, v68, v72, -v84
	v_fma_f32 v85, -v68, v73, -v85
	v_mul_f32_e32 v86, v71, v75
	v_mul_f32_e32 v87, v71, v74
	v_fma_f32 v86, v70, v74, -v86
	v_fma_f32 v87, -v70, v75, -v87
	s_waitcnt lgkmcnt(0)
	v_mul_f32_e32 v88, v77, v81
	v_mul_f32_e32 v89, v77, v80
	v_fma_f32 v88, v76, v80, -v88
	v_fma_f32 v89, -v76, v81, -v89
	v_mul_f32_e32 v90, v79, v83
	v_mul_f32_e32 v91, v79, v82
	v_fma_f32 v90, v78, v82, -v90
	v_fma_f32 v91, -v78, v83, -v91
	v_cvt_pk_bf16_f32 v84, v84, v85
	v_cvt_pk_bf16_f32 v85, v86, v87
	v_cvt_pk_bf16_f32 v86, v88, v89
	v_cvt_pk_bf16_f32 v87, v90, v91
	global_store_dwordx4 v64, v[84:87], s[6:7]
	s_add_u32 s6, s6, 0x1400
	s_addc_u32 s7, s7, 0
	s_add_i32 s8, s8, 1
	s_cmp_lt_u32 s8, 16
	s_cbranch_scc1 .Lp0_bssm_b
